# attention: unit index rotated so the 32 workgroups of an XCD work on two (batch, KV group) pairs (their K/V stay in that XCD's L2)
# baseline (speedup 1.0000x reference)
; #define LAS __attribute__((address_space(3)))
;     template <class Tp> __device__ __forceinline__ Tp* w(size_t off) const { return (Tp*)(ws + off); }
; __device__ __forceinline__ void ph_attn(const Frame& F) {
;     const nsa::Ptrs P{F.w<bf16>(WS_QN), F.w<bf16>(WS_KV6), F.w<float>(WS_GATE), F.w<bf16>(WS_KCB), F.w<bf16>(WS_VCB), F.i_rel_bias, F.w<bf16>(WS_MIXB)};
;     for (int su = blockIdx.x; su < 256; su += gridDim.x) { const int bg = su >> 4, j = su & 15;
;         for (int q = 0; q < 4; ++q) { const int c = q == 0 ? 63 - j : (q == 1 ? 32 + j : (q == 2 ? 31 - j : j)); nsa::attn_unit(P, (LAS char*)F.lds, F.tid, F.wave, bg >> 2, bg & 3, c, q == 0); } }
.LBB0_722:
	s_and_b32 s2, s97, 7
	s_lshl_b32 s2, s2, 5
	s_lshr_b32 s3, s97, 3
	s_or_b32 s3, s2, s3
	s_and_b32 s1, s3, 15
	v_writelane_b32 v248, s97, 49
	s_xor_b32 s4, s1, 31
	v_writelane_b32 v248, s4, 14
	s_or_b32 s4, s1, 32
	v_writelane_b32 v248, s4, 15
	s_ashr_i32 s0, s3, 6
	v_writelane_b32 v248, s1, 21
	s_xor_b32 s1, s1, 63
	v_writelane_b32 v248, s1, 16
	s_ashr_i32 s1, s0, 31
	s_bfe_u32 s2, s3, 0x20004
	s_lshl_b64 s[4:5], s[0:1], 12
	s_lshl_b32 s0, s0, 2
	v_writelane_b32 v248, s4, 19
	s_or_b32 s0, s0, s2
	s_mul_hi_i32 s1, s0, 0xff
	v_writelane_b32 v248, s5, 20
	s_mulk_i32 s0, 0xff
	v_writelane_b32 v248, s0, 17
	s_lshl_b32 s3, s2, 9
	s_lshl_b32 s74, s2, 2
	v_writelane_b32 v248, s1, 18
	s_lshl_b32 s0, s2, 4
	v_readlane_b32 s1, v248, 27
	s_add_u32 s4, s1, s0
	v_readlane_b32 s0, v248, 28
	s_addc_u32 s5, s0, 0
	v_writelane_b32 v248, s4, 7
	s_lshl_b32 s0, s2, 7
	s_mov_b32 s75, s74
	v_writelane_b32 v248, s5, 8
	s_mov_b32 s97, s87
	v_readlane_b32 s1, v248, 33
	s_add_u32 s4, s1, s0
	v_readlane_b32 s1, v248, 34
	s_addc_u32 s5, s1, 0
	v_writelane_b32 v248, s4, 50
	s_nop 1
	v_writelane_b32 v248, s5, 51
	s_nop 0
	v_readlane_b32 s1, v248, 37
	s_add_u32 s4, s1, s0
	v_readlane_b32 s1, v248, 38
	s_addc_u32 s5, s1, 0
	v_writelane_b32 v248, s4, 52
	s_nop 1
	v_writelane_b32 v248, s5, 53
	s_nop 0
	v_readlane_b32 s1, v248, 35
	s_add_u32 s4, s1, s0
	v_readlane_b32 s1, v248, 36
	s_addc_u32 s5, s1, 0
	v_writelane_b32 v248, s4, 54
	s_nop 1
	v_writelane_b32 v248, s5, 55
	s_nop 0
	v_readlane_b32 s1, v248, 39
	s_add_u32 s4, s1, s0
	v_readlane_b32 s0, v248, 40
	s_addc_u32 s5, s0, 0
	v_writelane_b32 v248, s4, 56
	s_nop 1
	v_writelane_b32 v248, s5, 57
	s_nop 0
	v_readlane_b32 s0, v248, 41
	s_add_u32 s2, s0, s3
	v_readlane_b32 s0, v248, 44
	s_addc_u32 s3, s0, 0
	v_writelane_b32 v248, s2, 58
	s_nop 1
	v_writelane_b32 v248, s3, 59
	s_branch .LBB0_724
